# attention block heads: recomputed uniform mask (v_cndmask + v_cmp_ne) replaced by one s_andn2_b64 at 4 sites
# baseline (speedup 1.0000x reference)
.LBB0_384:
	s_waitcnt lgkmcnt(0)
	s_barrier
	v_cndmask_b32_e64 v2, 0, 1, s[36:37]
	s_andn2_b64 s[10:11], exec, s[36:37]
	s_andn2_b64 vcc, exec, s[36:37]
	s_cbranch_vccnz .LBB0_387
	s_add_i32 s6, s82, -2
	s_cmp_gt_i32 s6, s62
	s_cbranch_scc1 .LBB0_387
	s_add_i32 s6, s83, 0xffffc000
	s_and_b32 s6, s6, 0x4000
	v_add_u32_e32 v2, s6, v213
	ds_read_b64_tr_b16 v[4:5], v2 offset:32768
	ds_read_b64_tr_b16 v[6:7], v2 offset:33280
	ds_read_b64_tr_b16 v[8:9], v2 offset:33792
	ds_read_b64_tr_b16 v[10:11], v2 offset:34304
	ds_read_b64_tr_b16 v[12:13], v2 offset:40960
	ds_read_b64_tr_b16 v[14:15], v2 offset:41472
	ds_read_b64_tr_b16 v[198:199], v2 offset:41984
	ds_read_b64_tr_b16 v[200:201], v2 offset:42496
	ds_read_b64_tr_b16 v[222:223], v2 offset:36864
	ds_read_b64_tr_b16 v[224:225], v2 offset:37376
	ds_read_b64_tr_b16 v[226:227], v2 offset:34816
	ds_read_b64_tr_b16 v[228:229], v2 offset:35328
	ds_read_b64_tr_b16 v[230:231], v2 offset:37888
	ds_read_b64_tr_b16 v[232:233], v2 offset:38400
	ds_read_b64_tr_b16 v[234:235], v2 offset:38912
	ds_read_b64_tr_b16 v[236:237], v2 offset:39424
	ds_read_b64_tr_b16 v[238:239], v2 offset:45056
	ds_read_b64_tr_b16 v[240:241], v2 offset:45568
	ds_read_b64_tr_b16 v[242:243], v2 offset:43008
	ds_read_b64_tr_b16 v[244:245], v2 offset:43520
	ds_read_b64_tr_b16 v[246:247], v2 offset:46080
	ds_read_b64_tr_b16 v[248:249], v2 offset:46592
	ds_read_b64_tr_b16 v[250:251], v2 offset:47104
	ds_read_b64_tr_b16 v[252:253], v2 offset:47616
	s_waitcnt lgkmcnt(14)
	v_mfma_f32_32x32x16_bf16 v[130:145], v[4:7], v[182:185], v[130:145]
	v_mfma_f32_32x32x16_bf16 v[98:113], v[222:225], v[182:185], v[98:113]
	v_mfma_f32_32x32x16_bf16 v[66:81], v[12:15], v[182:185], v[66:81]
	s_waitcnt lgkmcnt(6)
	v_mfma_f32_32x32x16_bf16 v[34:49], v[238:241], v[182:185], v[34:49]
	ds_read_b64_tr_b16 v[4:5], v2 offset:35840
	ds_read_b64_tr_b16 v[6:7], v2 offset:36352
	ds_read_b64_tr_b16 v[12:13], v2 offset:39936
	ds_read_b64_tr_b16 v[14:15], v2 offset:40448
	ds_read_b64_tr_b16 v[222:223], v2 offset:44032
	ds_read_b64_tr_b16 v[224:225], v2 offset:44544
	ds_read_b64_tr_b16 v[238:239], v2 offset:48128
	ds_read_b64_tr_b16 v[240:241], v2 offset:48640
	v_mfma_f32_32x32x16_bf16 v[130:145], v[8:11], v[186:189], v[130:145]
	v_mfma_f32_32x32x16_bf16 v[98:113], v[230:233], v[186:189], v[98:113]
	v_mfma_f32_32x32x16_bf16 v[66:81], v[198:201], v[186:189], v[66:81]
	s_waitcnt lgkmcnt(10)
	v_mfma_f32_32x32x16_bf16 v[34:49], v[246:249], v[186:189], v[34:49]
	v_mfma_f32_32x32x16_bf16 v[130:145], v[226:229], v[178:181], v[130:145]
	v_mfma_f32_32x32x16_bf16 v[98:113], v[234:237], v[178:181], v[98:113]
	v_mfma_f32_32x32x16_bf16 v[66:81], v[242:245], v[178:181], v[66:81]
	s_waitcnt lgkmcnt(8)
	v_mfma_f32_32x32x16_bf16 v[34:49], v[250:253], v[178:181], v[34:49]
	s_waitcnt lgkmcnt(6)
	v_mfma_f32_32x32x16_bf16 v[130:145], v[4:7], v[190:193], v[130:145]
	s_waitcnt lgkmcnt(4)
	v_mfma_f32_32x32x16_bf16 v[98:113], v[12:15], v[190:193], v[98:113]
	s_waitcnt lgkmcnt(2)
	v_mfma_f32_32x32x16_bf16 v[66:81], v[222:225], v[190:193], v[66:81]
	s_waitcnt lgkmcnt(0)
	v_mfma_f32_32x32x16_bf16 v[34:49], v[238:241], v[190:193], v[34:49]

.LBB0_393:
	v_cndmask_b32_e64 v2, 0, 1, s[36:37]
	s_andn2_b64 s[8:9], exec, s[36:37]
	s_andn2_b64 vcc, exec, s[36:37]
	s_cbranch_vccnz .LBB0_404
	s_cmp_le_i32 s80, s64
	s_cbranch_scc1 .LBB0_396
	v_add_u32_e32 v2, s81, v218
	v_add_u32_e32 v4, 0x206e0, v2
	v_add_u32_e32 v6, 0x20760, v2
	ds_read2_b32 v[4:5], v4 offset1:1
	ds_read2_b32 v[6:7], v6 offset1:1
	v_add_u32_e32 v8, 0x206e8, v2
	v_add_u32_e32 v10, 0x20768, v2
	v_add_u32_e32 v12, 0x20700, v2
	v_add_u32_e32 v14, 0x20780, v2
	v_add_u32_e32 v16, 0x20708, v2
	v_add_u32_e32 v178, 0x20788, v2
	v_add_u32_e32 v180, 0x20720, v2
	v_add_u32_e32 v182, 0x207a0, v2
	v_add_u32_e32 v184, 0x20728, v2
	v_add_u32_e32 v186, 0x207a8, v2
	v_add_u32_e32 v188, 0x20740, v2
	v_add_u32_e32 v190, 0x207c0, v2
	v_add_u32_e32 v192, 0x20748, v2
	v_add_u32_e32 v2, 0x207c8, v2
	ds_read2_b32 v[8:9], v8 offset1:1
	ds_read2_b32 v[10:11], v10 offset1:1
	ds_read2_b32 v[12:13], v12 offset1:1
	ds_read2_b32 v[14:15], v14 offset1:1
	ds_read2_b32 v[16:17], v16 offset1:1
	ds_read2_b32 v[178:179], v178 offset1:1
	ds_read2_b32 v[180:181], v180 offset1:1
	ds_read2_b32 v[182:183], v182 offset1:1
	ds_read2_b32 v[184:185], v184 offset1:1
	ds_read2_b32 v[186:187], v186 offset1:1
	ds_read2_b32 v[188:189], v188 offset1:1
	ds_read2_b32 v[190:191], v190 offset1:1
	ds_read2_b32 v[192:193], v192 offset1:1
	s_waitcnt lgkmcnt(14)
	v_add_f32_e32 v162, v162, v4
	v_add_f32_e32 v163, v163, v5
	ds_read2_b32 v[4:5], v2 offset1:1
	s_waitcnt lgkmcnt(3)
	v_add_f32_e32 v174, v174, v188
	v_add_f32_e32 v175, v175, v189
	v_add_f32_e32 v172, v172, v184
	v_add_f32_e32 v173, v173, v185
	s_waitcnt lgkmcnt(1)
	v_add_f32_e32 v176, v176, v192
	v_add_f32_e32 v177, v177, v193
	v_add_f32_e32 v170, v170, v180
	v_add_f32_e32 v171, v171, v181
	v_add_f32_e32 v168, v168, v16
	v_add_f32_e32 v169, v169, v17
	v_add_f32_e32 v166, v166, v12
	v_add_f32_e32 v167, v167, v13
	v_add_f32_e32 v164, v164, v8
	v_add_f32_e32 v165, v165, v9
	s_waitcnt lgkmcnt(0)
	v_add_f32_e32 v160, v160, v4
	v_add_f32_e32 v161, v161, v5
	v_add_f32_e32 v158, v158, v190
	v_add_f32_e32 v159, v159, v191
	v_add_f32_e32 v156, v156, v186
	v_add_f32_e32 v157, v157, v187
	v_add_f32_e32 v154, v154, v182
	v_add_f32_e32 v155, v155, v183
	v_add_f32_e32 v152, v152, v178
	v_add_f32_e32 v153, v153, v179
	v_add_f32_e32 v150, v150, v14
	v_add_f32_e32 v151, v151, v15
	v_add_f32_e32 v148, v148, v10
	v_add_f32_e32 v149, v149, v11
	v_add_f32_e32 v146, v146, v6
	v_add_f32_e32 v147, v147, v7

.LBB0_410:
	s_waitcnt vmcnt(0)
	s_waitcnt lgkmcnt(0)
	s_barrier
	v_cndmask_b32_e64 v2, 0, 1, s[58:59]
	s_andn2_b64 s[8:9], exec, s[58:59]
	s_andn2_b64 vcc, exec, s[58:59]
	s_cbranch_vccnz .LBB0_416
	v_readlane_b32 s6, v255, 32
	v_readlane_b32 s7, v255, 33
	s_andn2_b64 vcc, exec, s[6:7]
	v_mov_b32_e32 v219, v221
	s_cbranch_vccnz .LBB0_413
	v_or_b32_e32 v2, s97, v217
	v_sub_u32_e32 v2, 0xc0, v2
	s_add_i32 s6, 0, 0x20000
	v_lshlrev_b32_e32 v2, 2, v2
	v_lshlrev_b32_e32 v4, 2, v196
	v_add3_u32 v2, s6, v2, v4
	ds_read2_b32 v[4:5], v2 offset0:184 offset1:185
	ds_read2_b32 v[6:7], v2 offset0:186 offset1:187
	ds_read2_b32 v[8:9], v2 offset0:192 offset1:193
	ds_read2_b32 v[10:11], v2 offset0:194 offset1:195
	ds_read2_b32 v[12:13], v2 offset0:200 offset1:201
	ds_read2_b32 v[14:15], v2 offset0:202 offset1:203
	ds_read2_b32 v[16:17], v2 offset0:208 offset1:209
	ds_read2_b32 v[178:179], v2 offset0:210 offset1:211
	ds_read2_b32 v[180:181], v2 offset0:216 offset1:217
	ds_read2_b32 v[182:183], v2 offset0:218 offset1:219
	ds_read2_b32 v[184:185], v2 offset0:224 offset1:225
	ds_read2_b32 v[186:187], v2 offset0:226 offset1:227
	s_waitcnt lgkmcnt(4)
	v_add_f32_e32 v176, v176, v178
	v_add_f32_e32 v177, v177, v179
	v_add_f32_e32 v174, v174, v16
	v_add_f32_e32 v175, v175, v17
	v_add_f32_e32 v172, v172, v14
	v_add_f32_e32 v173, v173, v15
	v_add_f32_e32 v170, v170, v12
	v_add_f32_e32 v171, v171, v13
	ds_read2_b32 v[12:13], v2 offset0:232 offset1:233
	ds_read2_b32 v[14:15], v2 offset0:234 offset1:235
	ds_read2_b32 v[16:17], v2 offset0:240 offset1:241
	ds_read2_b32 v[178:179], v2 offset0:242 offset1:243
	v_add_f32_e32 v168, v168, v10
	v_add_f32_e32 v169, v169, v11
	v_add_f32_e32 v166, v166, v8
	v_add_f32_e32 v167, v167, v9
	v_add_f32_e32 v164, v164, v6
	v_add_f32_e32 v165, v165, v7
	v_add_f32_e32 v162, v162, v4
	v_add_f32_e32 v163, v163, v5
	s_waitcnt lgkmcnt(0)
	v_add_f32_e32 v160, v160, v178
	v_add_f32_e32 v161, v161, v179
	v_add_f32_e32 v158, v158, v16
	v_add_f32_e32 v159, v159, v17
	v_add_f32_e32 v156, v156, v14
	v_add_f32_e32 v157, v157, v15
	v_add_f32_e32 v154, v154, v12
	v_add_f32_e32 v155, v155, v13
	v_add_f32_e32 v152, v152, v186
	v_add_f32_e32 v153, v153, v187
	v_add_f32_e32 v150, v150, v184
	v_add_f32_e32 v151, v151, v185
	v_add_f32_e32 v148, v148, v182
	v_add_f32_e32 v149, v149, v183
	v_add_f32_e32 v146, v146, v180
	v_add_f32_e32 v147, v147, v181

.LBB0_432:
	s_waitcnt lgkmcnt(0)
	s_barrier
	v_cndmask_b32_e64 v2, 0, 1, s[10:11]
	s_andn2_b64 s[8:9], exec, s[10:11]
	s_andn2_b64 vcc, exec, s[10:11]
	s_cbranch_vccnz .LBB0_443
	s_cmp_le_i32 s65, s64
	s_cbranch_scc1 .LBB0_435
	v_add_u32_e32 v2, s38, v216
	v_add_u32_e32 v4, 0x206e0, v2
	v_add_u32_e32 v6, 0x20760, v2
	ds_read2_b32 v[4:5], v4 offset1:1
	ds_read2_b32 v[6:7], v6 offset1:1
	v_add_u32_e32 v8, 0x206e8, v2
	v_add_u32_e32 v10, 0x20768, v2
	v_add_u32_e32 v12, 0x20700, v2
	v_add_u32_e32 v14, 0x20780, v2
	v_add_u32_e32 v16, 0x20708, v2
	v_add_u32_e32 v178, 0x20788, v2
	v_add_u32_e32 v180, 0x20720, v2
	v_add_u32_e32 v182, 0x207a0, v2
	v_add_u32_e32 v184, 0x20728, v2
	v_add_u32_e32 v186, 0x207a8, v2
	v_add_u32_e32 v188, 0x20740, v2
	v_add_u32_e32 v190, 0x207c0, v2
	v_add_u32_e32 v192, 0x20748, v2
	v_add_u32_e32 v2, 0x207c8, v2
	ds_read2_b32 v[8:9], v8 offset1:1
	ds_read2_b32 v[10:11], v10 offset1:1
	ds_read2_b32 v[12:13], v12 offset1:1
	ds_read2_b32 v[14:15], v14 offset1:1
	ds_read2_b32 v[16:17], v16 offset1:1
	ds_read2_b32 v[178:179], v178 offset1:1
	ds_read2_b32 v[180:181], v180 offset1:1
	ds_read2_b32 v[182:183], v182 offset1:1
	ds_read2_b32 v[184:185], v184 offset1:1
	ds_read2_b32 v[186:187], v186 offset1:1
	ds_read2_b32 v[188:189], v188 offset1:1
	ds_read2_b32 v[190:191], v190 offset1:1
	ds_read2_b32 v[192:193], v192 offset1:1
	s_waitcnt lgkmcnt(14)
	v_add_f32_e32 v162, v162, v4
	v_add_f32_e32 v163, v163, v5
	ds_read2_b32 v[4:5], v2 offset1:1
	s_waitcnt lgkmcnt(3)
	v_add_f32_e32 v174, v174, v188
	v_add_f32_e32 v175, v175, v189
	v_add_f32_e32 v172, v172, v184
	v_add_f32_e32 v173, v173, v185
	s_waitcnt lgkmcnt(1)
	v_add_f32_e32 v176, v176, v192
	v_add_f32_e32 v177, v177, v193
	v_add_f32_e32 v170, v170, v180
	v_add_f32_e32 v171, v171, v181
	v_add_f32_e32 v168, v168, v16
	v_add_f32_e32 v169, v169, v17
	v_add_f32_e32 v166, v166, v12
	v_add_f32_e32 v167, v167, v13
	v_add_f32_e32 v164, v164, v8
	v_add_f32_e32 v165, v165, v9
	s_waitcnt lgkmcnt(0)
	v_add_f32_e32 v160, v160, v4
	v_add_f32_e32 v161, v161, v5
	v_add_f32_e32 v158, v158, v190
	v_add_f32_e32 v159, v159, v191
	v_add_f32_e32 v156, v156, v186
	v_add_f32_e32 v157, v157, v187
	v_add_f32_e32 v154, v154, v182
	v_add_f32_e32 v155, v155, v183
	v_add_f32_e32 v152, v152, v178
	v_add_f32_e32 v153, v153, v179
	v_add_f32_e32 v150, v150, v14
	v_add_f32_e32 v151, v151, v15
	v_add_f32_e32 v148, v148, v10
	v_add_f32_e32 v149, v149, v11
	v_add_f32_e32 v146, v146, v6
	v_add_f32_e32 v147, v147, v7
